# k_point gelu: same A&S erf formula with constants folded (u=fma(|x|,p*sqrt2/2,1), w=x*x*(-log2e/2), h+|h|=max(x,0), halved poly coefficients): 11 instead of 14 f32 op-equivalents per element; gelu is
# baseline (speedup 1.0000x reference)
.LBB0_10:
	s_or_b64 exec, exec, s[8:9]
	s_waitcnt vmcnt(16)
	v_add_u32_e32 v70, v1, v107
	v_pk_add_f32 v[60:61], v[60:61], v[64:65]
	v_pk_add_f32 v[58:59], v[58:59], v[62:63]
	v_cvt_pk_f16_f32 v61, v60, v61
	v_cvt_pk_f16_f32 v60, v58, v59
	v_or_b32_e32 v58, v95, v70
	v_pk_add_f32 v[52:53], v[52:53], v[56:57]
	v_pk_add_f32 v[50:51], v[50:51], v[54:55]
	v_or_b32_e32 v1, v1, v102
	v_lshlrev_b32_e32 v71, 3, v102
	s_add_i32 s6, 0, 0x14300
	v_mul_u32_u24_e32 v58, 0x88, v58
	v_cvt_pk_f16_f32 v53, v52, v53
	v_cvt_pk_f16_f32 v52, v50, v51
	v_mul_u32_u24_e32 v1, 0x88, v1
	v_lshlrev_b32_e32 v50, 3, v95
	v_lshlrev_b32_e32 v93, 2, v95
	v_add3_u32 v58, s6, v71, v58
	v_add3_u32 v1, s6, v1, v50
	v_lshrrev_b32_e32 v50, 2, v102
	v_and_b32_e32 v87, 4, v93
	ds_write2_b64 v58, v[60:61], v[52:53] offset1:68
	v_or_b32_e32 v52, v87, v50
	v_or_b32_e32 v50, v93, v50
	s_movk_i32 s6, 0x2d00
	v_lshlrev_b32_e32 v95, 2, v102
	v_mul_u32_u24_e32 v50, 0x50, v50
	s_waitcnt lgkmcnt(0)
	s_barrier
	ds_read2_b64 v[54:57], v1 offset1:4
	ds_read2_b64 v[62:65], v1 offset0:8 offset1:12
	v_mad_u32_u24 v86, v104, s6, 0
	v_and_b32_e32 v51, 12, v95
	v_lshlrev_b32_e32 v88, 1, v50
	v_mul_u32_u24_e32 v91, 0x50, v52
	v_lshlrev_b32_e32 v92, 1, v51
	v_add_u32_e32 v121, v86, v88
	v_mul_u32_u24_e32 v1, 0x140, v104
	s_add_i32 s11, 0, 0x10e00
	v_lshl_add_u32 v96, v91, 1, v86
	v_add_u32_e32 v100, v121, v92
	v_cndmask_b32_e64 v122, 32, 16, s[4:5]
	v_cmp_gt_u32_e64 s[20:21], v122, v103
	s_waitcnt vmcnt(12)
	s_nop 1
	v_cndmask_b32_e64 v66, 0, v66, s[20:21]
	v_cndmask_b32_e64 v67, 0, v67, s[20:21]
	v_cndmask_b32_e64 v68, 0, v68, s[20:21]
	v_cndmask_b32_e64 v69, 0, v69, s[20:21]
	v_cvt_pk_f16_f32 v66, v66, v67
	v_cvt_pk_f16_f32 v67, v68, v69
	v_add3_u32 v1, s11, v1, v108
	v_add_u32_e32 v107, v96, v92
	v_add3_u32 v120, v86, v92, v88
	ds_read_b64_tr_b16 v[52:53], v100 offset:2560
	ds_read_b64_tr_b16 v[50:51], v120
	ds_read_b64_tr_b16 v[58:59], v120 offset:32
	ds_read_b64_tr_b16 v[68:69], v120 offset:5120
	ds_read_b64_tr_b16 v[70:71], v100 offset:7680
	ds_read_b128 v[72:75], v1
	ds_read_b128 v[76:79], v1 offset:64
	ds_read_b64_tr_b16 v[80:81], v120 offset:5152
	ds_read_b64_tr_b16 v[98:99], v120 offset:5248
	s_waitcnt vmcnt(15)
	ds_read_b64_tr_b16 v[108:109], v120 offset:64
	s_waitcnt vmcnt(12)
	ds_read_b64_tr_b16 v[112:113], v120 offset:5184
	s_waitcnt lgkmcnt(5)
	v_mfma_f32_16x16x32_f16 v[72:75], v[50:53], v[54:57], v[72:75]
	ds_read_b64_tr_b16 v[50:51], v107 offset:10240
	v_mov_b32_e32 v52, 0
	v_mov_b32_e32 v53, v52
	ds_read_b64_tr_b16 v[60:61], v100 offset:2592
	ds_read_b64_tr_b16 v[84:85], v100 offset:2688
	v_mfma_f32_16x16x32_f16 v[70:73], v[68:71], v[62:65], v[72:75]
	v_mov_b32_e32 v68, v52
	v_mov_b32_e32 v69, v52
	ds_read_b128 v[116:119], v1 offset:256
	s_waitcnt lgkmcnt(2)
	v_mfma_f32_16x16x32_f16 v[58:61], v[58:61], v[54:57], v[76:79]
	s_mov_b32 s7, 0x3fb504f3
	s_mov_b32 s9, 0x3ea7ba05
	s_mov_b32 s8, 0xbfba00e3
	v_mfma_f32_16x16x32_f16 v[70:73], v[50:53], v[66:69], v[70:73]
	ds_read_b64_tr_b16 v[82:83], v100 offset:7712
	ds_read_b64_tr_b16 v[110:111], v100 offset:2624
	ds_read_b64_tr_b16 v[50:51], v107 offset:10304
	v_mov_b32_e32 v76, v52
	v_mov_b32_e32 v77, v52
	s_waitcnt lgkmcnt(2)
	v_mfma_f32_16x16x32_f16 v[58:61], v[80:83], v[62:65], v[58:61]
	ds_read_b64_tr_b16 v[74:75], v107 offset:10272
	ds_read_b64_tr_b16 v[114:115], v100 offset:7744
	ds_read_b64_tr_b16 v[100:101], v100 offset:7808
	s_mov_b32 s6, 0x3f87dc22
	s_mov_b32 s10, 0xbe91a98e
	s_waitcnt lgkmcnt(2)
	v_mfma_f32_16x16x32_f16 v[74:77], v[74:77], v[66:69], v[58:61]
	s_nop 2
	ds_read_b128 v[58:61], v1 offset:128
	ds_read_b128 v[78:81], v1 offset:192
	v_or_b32_e32 v1, 48, v95
	v_lshlrev_b32_e32 v95, 1, v1
	v_add3_u32 v1, v86, v95, v88
	s_waitcnt lgkmcnt(1)
	v_mfma_f32_16x16x32_f16 v[58:61], v[108:111], v[54:57], v[58:61]
	ds_read_b64_tr_b16 v[108:109], v1
	ds_read_b64_tr_b16 v[82:83], v120 offset:128
	v_add_u32_e32 v120, v121, v95
	ds_read_b64_tr_b16 v[110:111], v120 offset:2560
	v_mfma_f32_16x16x32_f16 v[58:61], v[112:115], v[62:65], v[58:61]
	s_mov_b32 s12, 0x3e827906
	v_mfma_f32_16x16x32_f16 v[112:115], v[50:53], v[66:69], v[58:61]
	s_nop 5
	ds_read_b64_tr_b16 v[60:61], v120 offset:7680
	ds_read_b64_tr_b16 v[58:59], v1 offset:5120
	v_add_u32_e32 v1, v96, v95
	ds_read_b64_tr_b16 v[50:51], v1 offset:10240
	s_waitcnt lgkmcnt(3)
	v_mfma_f32_16x16x32_f16 v[78:81], v[108:111], v[54:57], v[78:81]
	s_waitcnt lgkmcnt(1)
	v_mfma_f32_16x16x32_f16 v[58:61], v[58:61], v[62:65], v[78:81]
	s_waitcnt lgkmcnt(0)
	v_mfma_f32_16x16x32_f16 v[58:61], v[50:53], v[66:69], v[58:61]
	ds_read_b64_tr_b16 v[50:51], v107 offset:10368
	v_mfma_f32_16x16x32_f16 v[54:57], v[82:85], v[54:57], v[116:119]
	v_mfma_f32_16x16x32_f16 v[54:57], v[98:101], v[62:65], v[54:57]
	s_waitcnt lgkmcnt(0)
	v_mfma_f32_16x16x32_f16 v[54:57], v[50:53], v[66:69], v[54:57]
	s_mov_b32 s26, 0x3e6d3387
	s_mov_b32 s28, 0xbf38aa3b
	s_mov_b32 s30, 0x3f07dc22
	s_mov_b32 s32, 0xbf3a00e3
	s_mov_b32 s34, 0x3f35f0e3
	s_mov_b32 s36, 0xbe11a98e
	s_mov_b32 s38, 0x3e027906
	v_mov_b32_e32 v152, s32
	v_mov_b32_e32 v153, s32
	v_fma_f32 v124, |v70|, s26, 1.0
	v_fma_f32 v138, |v72|, s26, 1.0
	v_fma_f32 v125, |v71|, s26, 1.0
	v_fma_f32 v139, |v73|, s26, 1.0
	v_pk_mul_f32 v[126:127], v[70:71], s[28:29] op_sel_hi:[1,0]
	v_pk_mul_f32 v[140:141], v[72:73], s[28:29] op_sel_hi:[1,0]
	v_rcp_f32_e32 v124, v124
	v_rcp_f32_e32 v138, v138
	v_rcp_f32_e32 v125, v125
	v_rcp_f32_e32 v139, v139
	v_pk_mul_f32 v[128:129], v[126:127], v[70:71]
	v_pk_mul_f32 v[142:143], v[140:141], v[72:73]
	v_max_f32_e32 v132, 0, v70
	v_max_f32_e32 v146, 0, v72
	v_exp_f32_e32 v128, v128
	v_exp_f32_e32 v142, v142
	v_exp_f32_e32 v129, v129
	v_exp_f32_e32 v143, v143
	v_pk_fma_f32 v[130:131], v[124:125], s[30:31], v[152:153] op_sel_hi:[1,0,0]
	v_pk_fma_f32 v[144:145], v[138:139], s[30:31], v[152:153] op_sel_hi:[1,0,0]
	v_max_f32_e32 v133, 0, v71
	v_max_f32_e32 v147, 0, v73
	v_pk_fma_f32 v[130:131], v[130:131], v[124:125], s[34:35] op_sel_hi:[1,1,0]
	v_pk_fma_f32 v[144:145], v[144:145], v[138:139], s[34:35] op_sel_hi:[1,1,0]
	v_pk_fma_f32 v[130:131], v[130:131], v[124:125], s[36:37] op_sel_hi:[1,1,0]
	v_pk_fma_f32 v[144:145], v[144:145], v[138:139], s[36:37] op_sel_hi:[1,1,0]
	v_pk_fma_f32 v[130:131], v[130:131], v[124:125], s[38:39] op_sel_hi:[1,1,0]
	v_pk_fma_f32 v[144:145], v[144:145], v[138:139], s[38:39] op_sel_hi:[1,1,0]
	v_pk_mul_f32 v[130:131], v[124:125], v[130:131]
	v_pk_mul_f32 v[144:145], v[138:139], v[144:145]
	v_pk_mul_f32 v[130:131], v[128:129], v[130:131]
	v_pk_mul_f32 v[144:145], v[142:143], v[144:145]
	v_fma_f32 v62, -|v70|, v130, v132
	v_fma_f32 v64, -|v72|, v144, v146
	v_fma_f32 v63, -|v71|, v131, v133
	v_fma_f32 v65, -|v73|, v145, v147
	v_fma_f32 v124, |v74|, s26, 1.0
	v_fma_f32 v138, |v76|, s26, 1.0
	v_fma_f32 v125, |v75|, s26, 1.0
	v_fma_f32 v139, |v77|, s26, 1.0
	v_pk_mul_f32 v[126:127], v[74:75], s[28:29] op_sel_hi:[1,0]
	v_pk_mul_f32 v[140:141], v[76:77], s[28:29] op_sel_hi:[1,0]
	v_rcp_f32_e32 v124, v124
	v_rcp_f32_e32 v138, v138
	v_rcp_f32_e32 v125, v125
	v_rcp_f32_e32 v139, v139
	v_pk_mul_f32 v[128:129], v[126:127], v[74:75]
	v_pk_mul_f32 v[142:143], v[140:141], v[76:77]
	v_max_f32_e32 v132, 0, v74
	v_max_f32_e32 v146, 0, v76
	v_exp_f32_e32 v128, v128
	v_exp_f32_e32 v142, v142
	v_exp_f32_e32 v129, v129
	v_exp_f32_e32 v143, v143
	v_pk_fma_f32 v[130:131], v[124:125], s[30:31], v[152:153] op_sel_hi:[1,0,0]
	v_pk_fma_f32 v[144:145], v[138:139], s[30:31], v[152:153] op_sel_hi:[1,0,0]
	v_max_f32_e32 v133, 0, v75
	v_max_f32_e32 v147, 0, v77
	v_pk_fma_f32 v[130:131], v[130:131], v[124:125], s[34:35] op_sel_hi:[1,1,0]
	v_pk_fma_f32 v[144:145], v[144:145], v[138:139], s[34:35] op_sel_hi:[1,1,0]
	v_pk_fma_f32 v[130:131], v[130:131], v[124:125], s[36:37] op_sel_hi:[1,1,0]
	v_pk_fma_f32 v[144:145], v[144:145], v[138:139], s[36:37] op_sel_hi:[1,1,0]
	v_pk_fma_f32 v[130:131], v[130:131], v[124:125], s[38:39] op_sel_hi:[1,1,0]
	v_pk_fma_f32 v[144:145], v[144:145], v[138:139], s[38:39] op_sel_hi:[1,1,0]
	v_pk_mul_f32 v[130:131], v[124:125], v[130:131]
	v_pk_mul_f32 v[144:145], v[138:139], v[144:145]
	v_pk_mul_f32 v[130:131], v[128:129], v[130:131]
	v_pk_mul_f32 v[144:145], v[142:143], v[144:145]
	v_fma_f32 v74, -|v74|, v130, v132
	v_fma_f32 v76, -|v76|, v144, v146
	v_fma_f32 v75, -|v75|, v131, v133
	v_fma_f32 v77, -|v77|, v145, v147
	v_fma_f32 v124, |v112|, s26, 1.0
	v_fma_f32 v138, |v114|, s26, 1.0
	v_fma_f32 v125, |v113|, s26, 1.0
	v_fma_f32 v139, |v115|, s26, 1.0
	v_pk_mul_f32 v[126:127], v[112:113], s[28:29] op_sel_hi:[1,0]
	v_pk_mul_f32 v[140:141], v[114:115], s[28:29] op_sel_hi:[1,0]
	v_rcp_f32_e32 v124, v124
	v_rcp_f32_e32 v138, v138
	v_rcp_f32_e32 v125, v125
	v_rcp_f32_e32 v139, v139
	v_pk_mul_f32 v[128:129], v[126:127], v[112:113]
	v_pk_mul_f32 v[142:143], v[140:141], v[114:115]
	v_max_f32_e32 v132, 0, v112
	v_max_f32_e32 v146, 0, v114
	v_exp_f32_e32 v128, v128
	v_exp_f32_e32 v142, v142
	v_exp_f32_e32 v129, v129
	v_exp_f32_e32 v143, v143
	v_pk_fma_f32 v[130:131], v[124:125], s[30:31], v[152:153] op_sel_hi:[1,0,0]
	v_pk_fma_f32 v[144:145], v[138:139], s[30:31], v[152:153] op_sel_hi:[1,0,0]
	v_max_f32_e32 v133, 0, v113
	v_max_f32_e32 v147, 0, v115
	v_pk_fma_f32 v[130:131], v[130:131], v[124:125], s[34:35] op_sel_hi:[1,1,0]
	v_pk_fma_f32 v[144:145], v[144:145], v[138:139], s[34:35] op_sel_hi:[1,1,0]
	v_pk_fma_f32 v[130:131], v[130:131], v[124:125], s[36:37] op_sel_hi:[1,1,0]
	v_pk_fma_f32 v[144:145], v[144:145], v[138:139], s[36:37] op_sel_hi:[1,1,0]
	v_pk_fma_f32 v[130:131], v[130:131], v[124:125], s[38:39] op_sel_hi:[1,1,0]
	v_pk_fma_f32 v[144:145], v[144:145], v[138:139], s[38:39] op_sel_hi:[1,1,0]
	v_pk_mul_f32 v[130:131], v[124:125], v[130:131]
	v_pk_mul_f32 v[144:145], v[138:139], v[144:145]
	v_pk_mul_f32 v[130:131], v[128:129], v[130:131]
	v_pk_mul_f32 v[144:145], v[142:143], v[144:145]
	v_fma_f32 v78, -|v112|, v130, v132
	v_fma_f32 v80, -|v114|, v144, v146
	v_fma_f32 v79, -|v113|, v131, v133
	v_fma_f32 v81, -|v115|, v145, v147
	v_fma_f32 v124, |v58|, s26, 1.0
	v_fma_f32 v138, |v60|, s26, 1.0
	v_fma_f32 v125, |v59|, s26, 1.0
	v_fma_f32 v139, |v61|, s26, 1.0
	v_pk_mul_f32 v[126:127], v[58:59], s[28:29] op_sel_hi:[1,0]
	v_pk_mul_f32 v[140:141], v[60:61], s[28:29] op_sel_hi:[1,0]
	v_rcp_f32_e32 v124, v124
	v_rcp_f32_e32 v138, v138
	v_rcp_f32_e32 v125, v125
	v_rcp_f32_e32 v139, v139
	v_pk_mul_f32 v[128:129], v[126:127], v[58:59]
	v_pk_mul_f32 v[142:143], v[140:141], v[60:61]
	v_max_f32_e32 v132, 0, v58
	v_max_f32_e32 v146, 0, v60
	v_exp_f32_e32 v128, v128
	v_exp_f32_e32 v142, v142
	v_exp_f32_e32 v129, v129
	v_exp_f32_e32 v143, v143
	v_pk_fma_f32 v[130:131], v[124:125], s[30:31], v[152:153] op_sel_hi:[1,0,0]
	v_pk_fma_f32 v[144:145], v[138:139], s[30:31], v[152:153] op_sel_hi:[1,0,0]
	v_max_f32_e32 v133, 0, v59
	v_max_f32_e32 v147, 0, v61
	v_pk_fma_f32 v[130:131], v[130:131], v[124:125], s[34:35] op_sel_hi:[1,1,0]
	v_pk_fma_f32 v[144:145], v[144:145], v[138:139], s[34:35] op_sel_hi:[1,1,0]
	v_pk_fma_f32 v[130:131], v[130:131], v[124:125], s[36:37] op_sel_hi:[1,1,0]
	v_pk_fma_f32 v[144:145], v[144:145], v[138:139], s[36:37] op_sel_hi:[1,1,0]
	v_pk_fma_f32 v[130:131], v[130:131], v[124:125], s[38:39] op_sel_hi:[1,1,0]
	v_pk_fma_f32 v[144:145], v[144:145], v[138:139], s[38:39] op_sel_hi:[1,1,0]
	v_pk_mul_f32 v[130:131], v[124:125], v[130:131]
	v_pk_mul_f32 v[144:145], v[138:139], v[144:145]
	v_pk_mul_f32 v[130:131], v[128:129], v[130:131]
	v_pk_mul_f32 v[144:145], v[142:143], v[144:145]
	v_fma_f32 v58, -|v58|, v130, v132
	v_fma_f32 v60, -|v60|, v144, v146
	v_fma_f32 v59, -|v59|, v131, v133
	v_fma_f32 v61, -|v61|, v145, v147
	v_fma_f32 v124, |v54|, s26, 1.0
	v_fma_f32 v138, |v56|, s26, 1.0
	v_fma_f32 v125, |v55|, s26, 1.0
	v_fma_f32 v139, |v57|, s26, 1.0
	v_pk_mul_f32 v[126:127], v[54:55], s[28:29] op_sel_hi:[1,0]
	v_pk_mul_f32 v[140:141], v[56:57], s[28:29] op_sel_hi:[1,0]
	v_rcp_f32_e32 v124, v124
	v_rcp_f32_e32 v138, v138
	v_rcp_f32_e32 v125, v125
	v_rcp_f32_e32 v139, v139
	v_pk_mul_f32 v[128:129], v[126:127], v[54:55]
	v_pk_mul_f32 v[142:143], v[140:141], v[56:57]
	v_max_f32_e32 v132, 0, v54
	v_max_f32_e32 v146, 0, v56
	v_exp_f32_e32 v128, v128
	v_exp_f32_e32 v142, v142
	v_exp_f32_e32 v129, v129
	v_exp_f32_e32 v143, v143
	v_pk_fma_f32 v[130:131], v[124:125], s[30:31], v[152:153] op_sel_hi:[1,0,0]
	v_pk_fma_f32 v[144:145], v[138:139], s[30:31], v[152:153] op_sel_hi:[1,0,0]
	v_max_f32_e32 v133, 0, v55
	v_max_f32_e32 v147, 0, v57
	v_pk_fma_f32 v[130:131], v[130:131], v[124:125], s[34:35] op_sel_hi:[1,1,0]
	v_pk_fma_f32 v[144:145], v[144:145], v[138:139], s[34:35] op_sel_hi:[1,1,0]
	v_pk_fma_f32 v[130:131], v[130:131], v[124:125], s[36:37] op_sel_hi:[1,1,0]
	v_pk_fma_f32 v[144:145], v[144:145], v[138:139], s[36:37] op_sel_hi:[1,1,0]
	v_pk_fma_f32 v[130:131], v[130:131], v[124:125], s[38:39] op_sel_hi:[1,1,0]
	v_pk_fma_f32 v[144:145], v[144:145], v[138:139], s[38:39] op_sel_hi:[1,1,0]
	v_pk_mul_f32 v[130:131], v[124:125], v[130:131]
	v_pk_mul_f32 v[144:145], v[138:139], v[144:145]
	v_pk_mul_f32 v[130:131], v[128:129], v[130:131]
	v_pk_mul_f32 v[144:145], v[142:143], v[144:145]
	v_fma_f32 v82, -|v54|, v130, v132
	v_fma_f32 v84, -|v56|, v144, v146
	v_fma_f32 v83, -|v55|, v131, v133
	v_fma_f32 v85, -|v57|, v145, v147
	v_cvt_pk_f16_f32 v73, v60, v61
	v_cvt_pk_f16_f32 v71, v80, v81
	v_cvt_pk_f16_f32 v70, v78, v79
	v_cvt_pk_f16_f32 v72, v58, v59
	v_cvt_pk_f16_f32 v69, v76, v77
	v_lshlrev_b32_e32 v50, 1, v93
	v_cvt_pk_f16_f32 v67, v64, v65
	v_cvt_pk_f16_f32 v66, v62, v63
	v_cvt_pk_f16_f32 v68, v74, v75
	s_and_saveexec_b64 s[6:7], s[4:5]
	s_xor_b64 s[6:7], exec, s[6:7]
	s_cbranch_execz .LBB0_14
	s_movk_i32 s10, 0x48
	v_mul_lo_u32 v0, v97, s10
	v_ashrrev_i32_e32 v1, 31, v0
	v_mov_b32_e32 v51, v52
	s_waitcnt lgkmcnt(0)
	v_lshl_add_u64 v[0:1], v[0:1], 1, s[64:65]
	v_lshl_add_u64 v[0:1], v[0:1], 0, v[50:51]
	v_cvt_pk_f16_f32 v55, v64, v65
	v_cvt_pk_f16_f32 v54, v62, v63
	global_store_dwordx2 v[0:1], v[54:55], off
	v_cvt_pk_f16_f32 v55, v76, v77
	v_cvt_pk_f16_f32 v54, v74, v75
	global_store_dwordx2 v[0:1], v[54:55], off offset:32
	v_cvt_pk_f16_f32 v55, v80, v81
	v_cvt_pk_f16_f32 v54, v78, v79
	v_cmp_gt_u32_e64 s[4:5], 32, v103
	global_store_dwordx2 v[0:1], v[54:55], off offset:64
	v_cvt_pk_f16_f32 v55, v60, v61
	v_cvt_pk_f16_f32 v54, v58, v59
	global_store_dwordx2 v[0:1], v[54:55], off offset:96
	s_and_saveexec_b64 s[8:9], s[4:5]
	s_cbranch_execz .LBB0_13
	v_cvt_pk_f16_f32 v55, v84, v85
	v_cvt_pk_f16_f32 v54, v82, v83
	global_store_dwordx2 v[0:1], v[54:55], off offset:128
